# speedup vs baseline: 1.0417x; 1.0417x over previous
.LBB1_3:
	s_setprio 2
	s_load_dwordx8 s[4:11], s[0:1], 0x8
	s_lshr_b32 s16, s13, 6
	s_mul_i32 s14, s16, 0x1800
	s_mov_b32 s15, 0
	s_lshl_b64 s[18:19], s[14:15], 4
	v_and_b32_e32 v2, 63, v0
	s_waitcnt lgkmcnt(0)
	s_lshl_b32 s24, s12, 7
	s_add_u32 s21, s6, s24
	s_add_u32 s22, s8, s24
	s_add_u32 s23, s10, s24
	s_sub_u32 s21, s21, 0x20100
	s_sub_u32 s22, s22, 0x22100
	s_sub_u32 s23, s23, 0x24100
	s_add_u32 s4, s4, s18
	s_addc_u32 s5, s5, s19
	v_lshlrev_b32_e32 v54, 4, v2
	v_mov_b32_e32 v55, 0
	v_lshl_add_u64 v[18:19], s[4:5], 0, v[54:55]
	s_bfe_u32 s4, s2, 0x40003
	s_mul_i32 s14, s4, 0x1800
	v_lshl_add_u64 v[20:21], v[18:19], 0, s[14:15]
	global_load_dwordx4 v[2:5], v[20:21], off offset:2048
	global_load_dwordx4 v[6:9], v[20:21], off
	global_load_dwordx4 v[10:13], v[20:21], off offset:1024
	v_lshrrev_b32_e32 v14, 1, v0
	v_bfe_u32 v56, v0, 4, 2
	v_lshlrev_b32_e32 v54, 7, v1
	v_bitop3_b32 v14, v56, v14, 7 bitop3:0x78
	v_lshl_or_b32 v57, v14, 4, v54
	global_load_dwordx4 v[14:17], v[20:21], off offset:3072
	s_movk_i32 s2, 0x1000
	s_add_i32 s5, s3, 1
	s_and_b32 s5, s5, 15
	v_add_co_u32_e32 v44, vcc, s2, v20
	s_mul_i32 s14, s5, 0x1800
	s_nop 0
	v_addc_co_u32_e32 v45, vcc, 0, v21, vcc
	v_lshl_add_u64 v[46:47], v[18:19], 0, s[14:15]
	global_load_dwordx4 v[20:23], v[44:45], off
	global_load_dwordx4 v[24:27], v[44:45], off offset:1024
	global_load_dwordx4 v[28:31], v[46:47], off
	global_load_dwordx4 v[32:35], v[46:47], off offset:1024
	global_load_dwordx4 v[36:39], v[46:47], off offset:2048
	global_load_dwordx4 v[40:43], v[46:47], off offset:3072
	s_add_i32 s13, s3, 2
	s_and_b32 s13, s13, 15
	v_add_co_u32_e32 v52, vcc, s2, v46
	s_mul_i32 s14, s13, 0x1800
	s_nop 0
	v_addc_co_u32_e32 v53, vcc, 0, v47, vcc
	v_lshl_add_u64 v[58:59], v[18:19], 0, s[14:15]
	global_load_dwordx4 v[44:47], v[52:53], off
	global_load_dwordx4 v[48:51], v[52:53], off offset:1024
	global_load_dwordx4 v[60:63], v[58:59], off
	global_load_dwordx4 v[64:67], v[58:59], off offset:1024
	global_load_dwordx4 v[68:71], v[58:59], off offset:2048
	global_load_dwordx4 v[72:75], v[58:59], off offset:3072
	v_add_co_u32_e32 v52, vcc, s2, v58
	s_add_i32 s5, s3, 3
	s_nop 0
	v_addc_co_u32_e32 v53, vcc, 0, v59, vcc
	global_load_dwordx4 v[76:79], v[52:53], off
	global_load_dwordx4 v[80:83], v[52:53], off offset:1024
